# prologue role split refined: helper CUs also run the table steps and 3/4 of the x conversion rows
# baseline (speedup 1.0000x reference)
.LBB0_898:
	s_lshl_b32 s8, s43, 3
	s_add_i32 s8, s8, s91
	s_lshl_b32 s10, s42, 3
	s_movk_i32 s99, 0x3fff
	s_cmp_lg_u32 s42, 0x100
	s_cbranch_scc1 .Lp0_xs_done
	s_and_b32 s98, s43, 31
	s_lshr_b32 s8, s43, 5
	s_movk_i32 s42, 64
	s_cmp_lt_u32 s98, 8
	s_cbranch_scc1 .Lp0_xs_B
	s_mul_i32 s8, s8, 24
	s_add_i32 s8, s8, s98
	s_add_i32 s8, s8, -8
	s_lshl_b32 s8, s8, 3
	s_add_i32 s8, s8, s91
	s_addk_i32 s8, 0x3000
	s_movk_i32 s10, 0x600
	s_movk_i32 s43, 0x100
	s_branch .Lp0_xs_done
.Lp0_xs_B:
	s_lshl_b32 s8, s8, 3
	s_add_i32 s43, s8, s98
	s_lshl_b32 s8, s43, 3
	s_add_i32 s8, s8, s91
	s_movk_i32 s10, 0x200
	s_movk_i32 s99, 0x2fff
